# gate-merge br==2 epilogue: agent-scope L1 invalidate (buffer_inv sc1) replaced by L1-bypassing sc1 loads of the z0/z1 tiles this workgroup stored itself; on top of Y prefetch + SEL optimisations
# speedup vs baseline: 1.0165x; 1.0165x over previous
; #define PG8_LAS __attribute__((address_space(3)))
;     __device__ __forceinline__ void operator()(const f32x4 (&acc)[2][2][4][2], const Unit& u, int wr, int wc, int fr, int fq) const {
;         const int br = u.pn >> 2, pc = u.pn & 3;
;         const int row0 = u.pm * BM + wr * 64 + fr; const int col0 = pc * BM + wc * 32 + 8 * fq;
;         if (br == 2) { __builtin_amdgcn_fence(__ATOMIC_ACQUIRE, "agent"); }
;         const int b = (u.pm * BM) / SEQ; float rs[2][4]; row_rstd(u, wr, fr, rs);
;         f32x4 bv[2][2];
; #pragma unroll
;         for (int bj = 0; bj < 2; ++bj)
; #pragma unroll
;             for (int n = 0; n < 2; ++n) bv[bj][n] = *(const PG8_LAS f32x4*)(uintptr_t)(CV_LDS + u.idx * 1024 + (wc * 32 + 8 * fq + bj * HALF + 4 * n) * 4);
;         f32x4 sv[2][2];
;         if constexpr (I8) {
; #pragma unroll
;             for (int bj = 0; bj < 2; ++bj)
; #pragma unroll
;                 for (int n = 0; n < 2; ++n) sv[bj][n] = *(const PG8_LAS f32x4*)(uintptr_t)(SB_LDS + u.idx * 1024 + (wc * 32 + 8 * fq + bj * HALF + 4 * n) * 4); }
;         f16* Yb = Y + (size_t)br * YSTR;
; #pragma unroll
;         for (int ai = 0; ai < 2; ++ai) {
;             const int rowa = row0 + ai * HALF; const size_t offa = (size_t)rowa * 1024 + (size_t)(rowa >> 12) * GAPY + col0;
; #pragma unroll
;             for (int mp = 0; mp < 2; ++mp) {
;             f16x8 yv[4][2];
; #pragma unroll
;             for (int m = 2 * mp; m < 2 * mp + 2; ++m)
; #pragma unroll
;                 for (int bj = 0; bj < 2; ++bj) yv[m][bj] = *(const g_f16x8*)(Yb + offa + (size_t)m * 16 * 1024 + bj * HALF);
; #pragma unroll
;             for (int m = 2 * mp; m < 2 * mp + 2; ++m) { const size_t off = offa + (size_t)m * 16 * 1024;
;                 f16x8 za[2], zb[2];
;                 if (br == 2) {
; #pragma unroll
;                     for (int bj = 0; bj < 2; ++bj) { za[bj] = *(const g_f16x8*)(Y + off + bj * HALF); zb[bj] = *(const g_f16x8*)(Y + YSTR + off + bj * HALF); } }
.LBB0_1226:
	s_ashr_i32 s36, s47, 2
	s_cmp_eq_u32 s36, 2
	s_cselect_b64 s[38:39], -1, 0
	s_cmp_lg_u32 s36, 2
	s_cselect_b64 s[50:51], -1, 0
	s_and_b64 vcc, exec, s[50:51]
	s_cbranch_vccnz .LBB0_1228
	s_waitcnt vmcnt(0)
	s_nop 0
.LBB0_1228:
	s_lshl_b32 s37, s47, 8
	s_and_b32 s37, s37, 0x300
	v_lshl_add_u32 v218, s26, 8, v208
	v_add_u32_e32 v216, s37, v237
	s_lshl_b32 s46, s46, 10
	s_ashr_i32 s37, s36, 31
	v_ashrrev_i32_e32 v219, 31, v218
	s_add_i32 s47, s46, s87
	s_lshl_b64 s[36:37], s[36:37], 23
	v_ashrrev_i32_e32 v217, 31, v216
	v_lshlrev_b64 v[26:27], 10, v[218:219]
	s_add_u32 s48, s40, s36
	v_ashrrev_i32_e32 v28, 12, v218
	v_lshl_add_u64 v[26:27], v[26:27], 0, v[216:217]
	s_mov_b32 s26, 0xc00000
	s_addc_u32 s49, s41, s37
	v_mad_i64_i32 v[228:229], s[36:37], v28, s26, v[26:27]
	v_lshl_add_u64 v[224:225], v[228:229], 1, s[48:49]
	v_add_co_u32_e32 v26, vcc, 0x8000, v224
	global_load_dwordx4 v[190:193], v[224:225], off
	global_load_dwordx4 v[186:189], v[224:225], off offset:256
	v_addc_co_u32_e32 v27, vcc, 0, v225, vcc
	global_load_dwordx4 v[174:177], v[26:27], off
	global_load_dwordx4 v[162:165], v[26:27], off offset:256
	v_lshl_add_u32 v26, v197, 2, s47
	v_add_u32_e32 v26, 0x20000, v26
	ds_read2_b32 v[226:227], v26 offset1:16
	ds_read2_b32 v[220:221], v26 offset0:32 offset1:48
	ds_read2_b32 v[214:215], v26 offset0:128 offset1:144
	ds_read2_b32 v[212:213], v26 offset0:160 offset1:176
	v_add_u32_e32 v26, s46, v199
	v_add_u32_e32 v30, s46, v244
	ds_read_b128 v[62:65], v26
	ds_read_b128 v[50:53], v26 offset:16
	ds_read_b128 v[34:37], v26 offset:512
	ds_read_b128 v[26:29], v26 offset:528
	ds_read_b128 v[70:73], v30
	ds_read_b128 v[54:57], v30 offset:16
	ds_read_b128 v[38:41], v30 offset:512
	ds_read_b128 v[30:33], v30 offset:528
	v_cndmask_b32_e64 v42, 0, 1, s[38:39]
	v_cmp_ne_u32_e64 s[36:37], 1, v42
	v_bfrev_b32_e32 v211, 1
	s_andn2_b64 vcc, exec, s[38:39]
	s_cbranch_vccnz .LBB0_1230
	v_lshlrev_b64 v[42:43], 1, v[228:229]
	v_lshl_add_u64 v[44:45], s[40:41], 0, v[42:43]
	v_lshl_add_u64 v[46:47], s[44:45], 0, v[42:43]
	global_load_dwordx4 v[58:61], v[44:45], off sc1
	s_nop 0
	global_load_dwordx4 v[42:45], v[44:45], off offset:256 sc1
	s_nop 0
	global_load_dwordx4 v[66:69], v[46:47], off sc1
	s_nop 0
	global_load_dwordx4 v[46:49], v[46:47], off offset:256 sc1
	s_branch .LBB0_1231

;     __device__ __forceinline__ void operator()(const f32x4 (&acc)[2][2][4][2], const Unit& u, int wr, int wc, int fr, int fq) const {
;     ...
;             for (int m = 2 * mp; m < 2 * mp + 2; ++m) { const size_t off = offa + (size_t)m * 16 * 1024;
;                 f16x8 za[2], zb[2];
;                 if (br == 2) {
; #pragma unroll
;                     for (int bj = 0; bj < 2; ++bj) { za[bj] = *(const g_f16x8*)(Y + off + bj * HALF); zb[bj] = *(const g_f16x8*)(Y + YSTR + off + bj * HALF); } }
.LBB0_1239:
	v_cvt_pk_f16_f32 v180, v166, v167
	v_cvt_pk_f16_f32 v181, v172, v173
	v_cvt_pk_f16_f32 v182, v170, v171
	v_cvt_pk_f16_f32 v183, v168, v169
	s_and_b64 vcc, exec, s[36:37]
	global_store_dwordx4 v[178:179], v[180:183], off offset:256
	s_cbranch_vccnz .LBB0_1241
	v_mov_b64_e32 v[42:43], 0x8000
	v_lshl_add_u64 v[42:43], v[228:229], 1, v[42:43]
	v_lshl_add_u64 v[44:45], s[40:41], 0, v[42:43]
	s_waitcnt vmcnt(4)
	v_lshl_add_u64 v[46:47], s[44:45], 0, v[42:43]
	global_load_dwordx4 v[58:61], v[44:45], off sc1
	s_nop 0
	global_load_dwordx4 v[42:45], v[44:45], off offset:256 sc1
	s_nop 0
	global_load_dwordx4 v[66:69], v[46:47], off sc1
	s_nop 0
	global_load_dwordx4 v[46:49], v[46:47], off offset:256 sc1

;     __device__ __forceinline__ void operator()(const f32x4 (&acc)[2][2][4][2], const Unit& u, int wr, int wc, int fr, int fq) const {
;     ...
;             for (int mp = 0; mp < 2; ++mp) {
;             f16x8 yv[4][2];
; #pragma unroll
;             for (int m = 2 * mp; m < 2 * mp + 2; ++m)
; #pragma unroll
;                 for (int bj = 0; bj < 2; ++bj) yv[m][bj] = *(const g_f16x8*)(Yb + offa + (size_t)m * 16 * 1024 + bj * HALF);
; #pragma unroll
;             for (int m = 2 * mp; m < 2 * mp + 2; ++m) { const size_t off = offa + (size_t)m * 16 * 1024;
;                 f16x8 za[2], zb[2];
;                 if (br == 2) {
; #pragma unroll
;                     for (int bj = 0; bj < 2; ++bj) { za[bj] = *(const g_f16x8*)(Y + off + bj * HALF); zb[bj] = *(const g_f16x8*)(Y + YSTR + off + bj * HALF); } }
.LBB0_1247:
	s_mov_b64 s[28:29], 0x8000
	v_lshl_add_u64 v[158:159], v[178:179], 0, s[28:29]
	v_cvt_pk_f16_f32 v154, v146, v147
	v_cvt_pk_f16_f32 v155, v152, v153
	v_cvt_pk_f16_f32 v156, v150, v151
	v_cvt_pk_f16_f32 v157, v148, v149
	v_add_co_u32_e32 v146, vcc, 0x10000, v224
	global_store_dwordx4 v[158:159], v[154:157], off offset:256
	s_nop 0
	v_addc_co_u32_e32 v147, vcc, 0, v225, vcc
	v_add_co_u32_e32 v146, vcc, 0x18000, v224
	s_nop 1
	v_addc_co_u32_e32 v147, vcc, 0, v225, vcc
	global_load_dwordx4 v[150:153], v[146:147], off
	s_nop 0
	global_load_dwordx4 v[146:149], v[146:147], off offset:256
	v_lshl_add_u64 v[222:223], v[228:229], 1, s[48:49]
	s_mov_b64 s[28:29], 0x40000
	v_lshl_add_u64 v[222:223], v[222:223], 0, s[28:29]
	global_load_dwordx4 v[174:177], v[222:223], off
	global_load_dwordx4 v[180:183], v[222:223], off offset:256
	s_and_b64 vcc, exec, s[36:37]
	s_cbranch_vccnz .LBB0_1249
	v_mov_b64_e32 v[42:43], 0x10000
	v_lshl_add_u64 v[42:43], v[228:229], 1, v[42:43]
	v_lshl_add_u64 v[44:45], s[40:41], 0, v[42:43]
	s_waitcnt vmcnt(6)
	v_lshl_add_u64 v[46:47], s[44:45], 0, v[42:43]
	global_load_dwordx4 v[58:61], v[44:45], off sc1
	s_nop 0
	global_load_dwordx4 v[42:45], v[44:45], off offset:256 sc1
	s_nop 0
	global_load_dwordx4 v[66:69], v[46:47], off sc1
	s_nop 0
	global_load_dwordx4 v[46:49], v[46:47], off offset:256 sc1

;     __device__ __forceinline__ void operator()(const f32x4 (&acc)[2][2][4][2], const Unit& u, int wr, int wc, int fr, int fq) const {
;     ...
;             for (int mp = 0; mp < 2; ++mp) {
;             f16x8 yv[4][2];
; #pragma unroll
;             for (int m = 2 * mp; m < 2 * mp + 2; ++m)
; #pragma unroll
;                 for (int bj = 0; bj < 2; ++bj) yv[m][bj] = *(const g_f16x8*)(Yb + offa + (size_t)m * 16 * 1024 + bj * HALF);
; #pragma unroll
;             for (int m = 2 * mp; m < 2 * mp + 2; ++m) { const size_t off = offa + (size_t)m * 16 * 1024;
;                 f16x8 za[2], zb[2];
;                 if (br == 2) {
; #pragma unroll
;                     for (int bj = 0; bj < 2; ++bj) { za[bj] = *(const g_f16x8*)(Y + off + bj * HALF); zb[bj] = *(const g_f16x8*)(Y + YSTR + off + bj * HALF); } }
.LBB0_1255:
	s_mov_b64 s[28:29], 0x10000
	v_lshl_add_u64 v[142:143], v[178:179], 0, s[28:29]
	v_cvt_pk_f16_f32 v138, v130, v131
	v_cvt_pk_f16_f32 v139, v136, v137
	v_cvt_pk_f16_f32 v140, v134, v135
	v_cvt_pk_f16_f32 v141, v132, v133
	s_and_b64 vcc, exec, s[36:37]
	global_store_dwordx4 v[142:143], v[138:141], off offset:256
	v_lshl_add_u64 v[222:223], v[228:229], 1, s[48:49]
	s_mov_b64 s[28:29], 0x48000
	v_lshl_add_u64 v[222:223], v[222:223], 0, s[28:29]
	global_load_dwordx4 v[162:165], v[222:223], off
	global_load_dwordx4 v[166:169], v[222:223], off offset:256
	s_cbranch_vccnz .LBB0_1257
	v_mov_b64_e32 v[42:43], 0x18000
	v_lshl_add_u64 v[42:43], v[228:229], 1, v[42:43]
	v_lshl_add_u64 v[44:45], s[40:41], 0, v[42:43]
	s_waitcnt vmcnt(4)
	v_lshl_add_u64 v[46:47], s[44:45], 0, v[42:43]
	global_load_dwordx4 v[58:61], v[44:45], off sc1
	s_nop 0
	global_load_dwordx4 v[42:45], v[44:45], off offset:256 sc1
	s_nop 0
	global_load_dwordx4 v[66:69], v[46:47], off sc1
	s_nop 0
	global_load_dwordx4 v[46:49], v[46:47], off offset:256 sc1

;     __device__ __forceinline__ void operator()(const f32x4 (&acc)[2][2][4][2], const Unit& u, int wr, int wc, int fr, int fq) const {
;     ...
;             const int rowa = row0 + ai * HALF; const size_t offa = (size_t)rowa * 1024 + (size_t)(rowa >> 12) * GAPY + col0;
; #pragma unroll
;             for (int mp = 0; mp < 2; ++mp) {
;             f16x8 yv[4][2];
; #pragma unroll
;             for (int m = 2 * mp; m < 2 * mp + 2; ++m)
; #pragma unroll
;                 for (int bj = 0; bj < 2; ++bj) yv[m][bj] = *(const g_f16x8*)(Yb + offa + (size_t)m * 16 * 1024 + bj * HALF);
; #pragma unroll
;             for (int m = 2 * mp; m < 2 * mp + 2; ++m) { const size_t off = offa + (size_t)m * 16 * 1024;
;                 f16x8 za[2], zb[2];
;                 if (br == 2) {
; #pragma unroll
;                     for (int bj = 0; bj < 2; ++bj) { za[bj] = *(const g_f16x8*)(Y + off + bj * HALF); zb[bj] = *(const g_f16x8*)(Y + YSTR + off + bj * HALF); } }
.LBB0_1263:
	v_cvt_pk_f16_f32 v122, v114, v115
	v_add_u32_e32 v114, 0x80, v218
	v_ashrrev_i32_e32 v115, 31, v114
	v_cvt_pk_f16_f32 v125, v116, v117
	v_lshlrev_b64 v[116:117], 10, v[114:115]
	v_cvt_pk_f16_f32 v124, v118, v119
	v_ashrrev_i32_e32 v118, 12, v114
	v_lshl_add_u64 v[114:115], v[116:117], 0, v[216:217]
	s_mov_b32 s26, 0xc00000
	v_mad_i64_i32 v[130:131], s[50:51], v118, s26, v[114:115]
	s_mov_b64 s[28:29], 0x18000
	v_lshl_add_u64 v[132:133], v[130:131], 1, s[48:49]
	v_lshl_add_u64 v[126:127], v[178:179], 0, s[28:29]
	v_cvt_pk_f16_f32 v123, v120, v121
	v_add_co_u32_e32 v114, vcc, 0x8000, v132
	global_store_dwordx4 v[126:127], v[122:125], off offset:256
	v_lshl_add_u64 v[222:223], v[228:229], 1, s[48:49]
	s_mov_b64 s[28:29], 0x50000
	v_lshl_add_u64 v[222:223], v[222:223], 0, s[28:29]
	global_load_dwordx4 v[146:149], v[222:223], off
	global_load_dwordx4 v[150:153], v[222:223], off offset:256
	v_lshl_add_u64 v[222:223], v[228:229], 1, s[48:49]
	s_mov_b64 s[28:29], 0x58000
	v_lshl_add_u64 v[222:223], v[222:223], 0, s[28:29]
	global_load_dwordx4 v[154:157], v[222:223], off
	global_load_dwordx4 v[158:161], v[222:223], off offset:256
	s_nop 0
	v_addc_co_u32_e32 v115, vcc, 0, v133, vcc
	s_nop 0
	s_and_b64 vcc, exec, s[36:37]
	s_cbranch_vccnz .LBB0_1265
	v_lshlrev_b64 v[42:43], 1, v[130:131]
	v_lshl_add_u64 v[44:45], s[40:41], 0, v[42:43]
	s_waitcnt vmcnt(6)
	v_lshl_add_u64 v[46:47], s[44:45], 0, v[42:43]
	global_load_dwordx4 v[58:61], v[44:45], off sc1
	s_nop 0
	global_load_dwordx4 v[42:45], v[44:45], off offset:256 sc1
	s_nop 0
	global_load_dwordx4 v[66:69], v[46:47], off sc1
	s_nop 0
	global_load_dwordx4 v[46:49], v[46:47], off offset:256 sc1

;     __device__ __forceinline__ void operator()(const f32x4 (&acc)[2][2][4][2], const Unit& u, int wr, int wc, int fr, int fq) const {
;     ...
;             for (int m = 2 * mp; m < 2 * mp + 2; ++m) { const size_t off = offa + (size_t)m * 16 * 1024;
;                 f16x8 za[2], zb[2];
;                 if (br == 2) {
; #pragma unroll
;                     for (int bj = 0; bj < 2; ++bj) { za[bj] = *(const g_f16x8*)(Y + off + bj * HALF); zb[bj] = *(const g_f16x8*)(Y + YSTR + off + bj * HALF); } }
.LBB0_1271:
	v_cvt_pk_f16_f32 v108, v98, v99
	v_cvt_pk_f16_f32 v109, v104, v105
	v_cvt_pk_f16_f32 v110, v102, v103
	v_cvt_pk_f16_f32 v111, v100, v101
	s_and_b64 vcc, exec, s[36:37]
	global_store_dwordx4 v[106:107], v[108:111], off offset:256
	s_cbranch_vccnz .LBB0_1273
	v_mov_b64_e32 v[42:43], 0x8000
	v_lshl_add_u64 v[42:43], v[130:131], 1, v[42:43]
	v_lshl_add_u64 v[44:45], s[40:41], 0, v[42:43]
	s_waitcnt vmcnt(2)
	v_lshl_add_u64 v[46:47], s[44:45], 0, v[42:43]
	global_load_dwordx4 v[58:61], v[44:45], off sc1
	s_nop 0
	global_load_dwordx4 v[42:45], v[44:45], off offset:256 sc1
	s_nop 0
	global_load_dwordx4 v[66:69], v[46:47], off sc1
	s_nop 0
	global_load_dwordx4 v[46:49], v[46:47], off offset:256 sc1

;     __device__ __forceinline__ void operator()(const f32x4 (&acc)[2][2][4][2], const Unit& u, int wr, int wc, int fr, int fq) const {
;     ...
;             for (int mp = 0; mp < 2; ++mp) {
;             f16x8 yv[4][2];
; #pragma unroll
;             for (int m = 2 * mp; m < 2 * mp + 2; ++m)
; #pragma unroll
;                 for (int bj = 0; bj < 2; ++bj) yv[m][bj] = *(const g_f16x8*)(Yb + offa + (size_t)m * 16 * 1024 + bj * HALF);
; #pragma unroll
;             for (int m = 2 * mp; m < 2 * mp + 2; ++m) { const size_t off = offa + (size_t)m * 16 * 1024;
;                 f16x8 za[2], zb[2];
;                 if (br == 2) {
; #pragma unroll
;                     for (int bj = 0; bj < 2; ++bj) { za[bj] = *(const g_f16x8*)(Y + off + bj * HALF); zb[bj] = *(const g_f16x8*)(Y + YSTR + off + bj * HALF); } }
.LBB0_1279:
	s_mov_b64 s[28:29], 0x8000
	v_lshl_add_u64 v[94:95], v[106:107], 0, s[28:29]
	v_cvt_pk_f16_f32 v90, v82, v83
	v_cvt_pk_f16_f32 v91, v88, v89
	v_cvt_pk_f16_f32 v92, v86, v87
	v_cvt_pk_f16_f32 v93, v84, v85
	v_add_co_u32_e32 v82, vcc, 0x10000, v132
	global_store_dwordx4 v[94:95], v[90:93], off offset:256
	s_nop 0
	v_addc_co_u32_e32 v83, vcc, 0, v133, vcc
	v_add_co_u32_e32 v82, vcc, 0x18000, v132
	s_nop 1
	v_addc_co_u32_e32 v83, vcc, 0, v133, vcc
	s_nop 0
	s_and_b64 vcc, exec, s[36:37]
	s_cbranch_vccnz .LBB0_1281
	v_mov_b64_e32 v[42:43], 0x10000
	v_lshl_add_u64 v[42:43], v[130:131], 1, v[42:43]
	v_lshl_add_u64 v[44:45], s[40:41], 0, v[42:43]
	s_waitcnt vmcnt(2)
	v_lshl_add_u64 v[46:47], s[44:45], 0, v[42:43]
	global_load_dwordx4 v[58:61], v[44:45], off sc1
	s_nop 0
	global_load_dwordx4 v[42:45], v[44:45], off offset:256 sc1
	s_nop 0
	global_load_dwordx4 v[66:69], v[46:47], off sc1
	s_nop 0
	global_load_dwordx4 v[46:49], v[46:47], off offset:256 sc1

;     __device__ __forceinline__ void operator()(const f32x4 (&acc)[2][2][4][2], const Unit& u, int wr, int wc, int fr, int fq) const {
;     ...
;             for (int m = 2 * mp; m < 2 * mp + 2; ++m) { const size_t off = offa + (size_t)m * 16 * 1024;
;                 f16x8 za[2], zb[2];
;                 if (br == 2) {
; #pragma unroll
;                     for (int bj = 0; bj < 2; ++bj) { za[bj] = *(const g_f16x8*)(Y + off + bj * HALF); zb[bj] = *(const g_f16x8*)(Y + YSTR + off + bj * HALF); } }
.LBB0_1287:
	s_mov_b64 s[28:29], 0x10000
	v_lshl_add_u64 v[78:79], v[106:107], 0, s[28:29]
	v_cvt_pk_f16_f32 v74, v18, v19
	v_cvt_pk_f16_f32 v75, v24, v25
	v_cvt_pk_f16_f32 v76, v22, v23
	v_cvt_pk_f16_f32 v77, v20, v21
	s_and_b64 vcc, exec, s[36:37]
	global_store_dwordx4 v[78:79], v[74:77], off offset:256
	s_cbranch_vccnz .LBB0_1289
	v_mov_b64_e32 v[18:19], 0x18000
	v_lshl_add_u64 v[18:19], v[130:131], 1, v[18:19]
	v_lshl_add_u64 v[20:21], s[40:41], 0, v[18:19]
	v_lshl_add_u64 v[18:19], s[44:45], 0, v[18:19]
	global_load_dwordx4 v[58:61], v[20:21], off sc1
	global_load_dwordx4 v[42:45], v[20:21], off offset:256 sc1
	global_load_dwordx4 v[66:69], v[18:19], off sc1
	global_load_dwordx4 v[46:49], v[18:19], off offset:256 sc1
